# speedup vs baseline: 1.0392x; 1.0115x over previous
.LBB1_39:
	s_or_b64 exec, exec, s[6:7]
	s_movk_i32 s3, 0xbf
	v_cmp_lt_u32_e64 s[6:7], s3, v0
	s_movk_i32 s3, 0xc0
	v_cmp_gt_u32_e32 vcc, s3, v0
	s_and_saveexec_b64 s[8:9], vcc
	s_setprio 3
	s_or_b64 exec, exec, s[8:9]
	v_mul_u32_u24_e32 v126, 0x90, v189
	s_add_i32 s16, 0, 0x24400
	v_lshlrev_b32_e32 v191, 2, v122
	v_lshl_add_u32 v126, v126, 1, 0
	v_lshlrev_b32_e32 v192, 3, v122
	v_lshlrev_b32_e32 v122, 4, v122
	v_lshl_or_b32 v127, v124, 4, v189
	v_lshl_add_u32 v196, v1, 4, s16
	s_movk_i32 s12, 0xff70
	v_lshlrev_b32_e32 v190, 4, v128
	v_add_u32_e32 v193, v126, v122
	v_mul_i32_i24_e32 v127, 0xd0, v127
	v_lshl_add_u32 v197, v124, 10, v196
	v_mad_i32_i24 v124, v189, s12, v126
	v_lshlrev_b32_e32 v126, 6, v128
	v_add3_u32 v194, 0, v127, v122
	v_mul_u32_u24_e32 v127, 0xe0, v189
	s_add_i32 s24, 0, 0x20c00
	v_add3_u32 v198, 0, v126, v122
	v_or_b32_e32 v126, v190, v189
	v_add3_u32 v195, s24, v127, v122
	v_mul_u32_u24_e32 v127, 0x110, v126
	v_add3_u32 v199, 0, v127, v122
	v_lshlrev_b32_e32 v127, 5, v128
	v_add3_u32 v200, v124, v127, v192
	v_lshl_add_u32 v132, v189, 6, v124
	v_add_u32_e32 v202, v124, v122
	v_or_b32_e32 v124, v191, v190
	s_movk_i32 s20, 0x50
	v_lshl_add_u32 v203, v0, 4, s16
	v_cmp_gt_u32_e64 s[16:17], 40, v124
	v_mad_u32_u24 v124, v189, s20, v132
	v_add3_u32 v205, v124, v127, v192
	v_add_u32_e32 v206, v124, v122
	v_and_b32_e32 v124, 0xc0, v0
	s_add_i32 s54, 0, 0x15400
	v_lshl_add_u32 v207, v124, 4, v196
	v_add_u16_e32 v124, -3, v128
	s_movk_i32 s22, 0xab
	v_add3_u32 v204, s54, v127, v192
	v_mul_lo_u16_sdwa v127, v124, s22 dst_sel:DWORD dst_unused:UNUSED_PAD src0_sel:BYTE_0 src1_sel:DWORD
	v_lshrrev_b16_e32 v127, 9, v127
	v_add_u32_e32 v201, v132, v122
	v_mul_lo_u16_e32 v132, 3, v127
	v_sub_u16_e32 v124, v124, v132
	v_and_b32_e32 v124, 0xff, v124
	v_lshl_or_b32 v132, v124, 4, v189
	v_mul_u32_u24_e32 v132, 0xd0, v132
	v_add3_u32 v208, 0, v132, v122
	v_lshl_or_b32 v132, v127, 4, v189
	v_mul_u32_u24_e32 v132, 0xe0, v132
	v_lshlrev_b32_e32 v117, 1, v117
	v_lshlrev_b32_e32 v121, 1, v121
	v_add3_u32 v209, s24, v132, v122
	v_mad_u32_u24 v124, v127, 3, v124
	v_add_u32_e32 v213, s24, v117
	v_add_u32_e32 v214, s24, v121
	s_add_i32 s24, 0, 0x1c400
	v_lshl_add_u32 v210, v124, 10, v196
	v_add_u32_e32 v124, 2, v128
	v_lshl_add_u32 v221, v115, 1, s24
	v_lshl_add_u32 v222, v116, 1, s24
	v_lshl_add_u32 v225, v114, 2, 0
	v_add_u32_e32 v227, s24, v122
	v_add3_u32 v114, v123, v131, v0
	s_mul_i32 s24, s2, 0x6900
	v_mul_u32_u24_e32 v115, 0x690, v130
	v_mul_lo_u16_e32 v127, 0x56, v124
	v_mov_b32_e32 v132, 3
	v_add3_u32 v114, v114, s24, v115
	v_min_u32_e32 v115, 0xc0, v0
	v_mul_lo_u16_sdwa v127, v127, v132 dst_sel:DWORD dst_unused:UNUSED_PAD src0_sel:BYTE_1 src1_sel:DWORD
	v_sub_u32_e32 v114, v114, v115
	v_sub_u16_e32 v127, v124, v127
	v_add_u32_e32 v154, 0x8c, v114
	v_add_u32_e32 v114, v125, v0
	v_mul_u32_u24_e32 v116, 0x690, v129
	v_lshlrev_b16_e32 v127, 4, v127
	s_movk_i32 s25, 0xf0
	v_add3_u32 v114, v114, s24, v116
	v_and_or_b32 v127, v127, s25, v189
	v_add_u32_e32 v224, s54, v121
	v_ashrrev_i32_e32 v121, 31, v120
	v_sub_u32_e32 v114, v114, v115
	s_mul_i32 s25, s2, 0x18000
	v_add_u32_e32 v156, 0x8c, v114
	v_lshl_add_u64 v[158:159], v[120:121], 2, s[40:41]
	v_lshl_add_u64 v[160:161], v[118:119], 2, s[40:41]
	s_movk_i32 s40, 0x1800
	v_mov_b32_e32 v114, s25
	v_mad_u32_u24 v114, v189, s40, v114
	v_or_b32_e32 v229, v114, v190
	v_mul_u32_u24_e32 v114, 0x690, v189
	v_add3_u32 v230, s24, v114, v190
	v_lshl_add_u32 v114, v128, 3, 0
	s_movk_i32 s10, 0x180
	v_cmp_eq_u32_e32 vcc, 2, v128
	v_cmp_gt_u32_e64 s[12:13], 16, v1
	v_lshlrev_b32_e32 v126, 7, v126
	s_movk_i32 s20, 0x300
	s_movk_i32 s22, 0x1c0
	v_mul_u32_u24_e32 v127, 0xd0, v127
	v_add_u32_e32 v231, 0x27400, v114
	v_mov_b32_e32 v114, 0
	s_movk_i32 s3, 0x90
	s_mov_b32 s33, 0
	v_cmp_ne_u32_e64 s[8:9], 3, v128
	v_cmp_gt_u32_e64 s[10:11], s10, v0
	s_movk_i32 s52, 0xd0
	s_movk_i32 s53, 0xe0
	s_and_b64 s[14:15], vcc, s[12:13]
	v_cmp_eq_u32_e64 s[18:19], 0, v1
	v_cmp_gt_u32_e64 s[20:21], s20, v0
	v_cmp_gt_u32_e64 s[22:23], s22, v0
	v_add3_u32 v211, 0, v127, v122
	v_lshl_add_u32 v212, v124, 10, v196
	v_add_u32_e32 v215, 0xe00, v213
	v_add_u32_e32 v216, 0x1c00, v213
	v_add_u32_e32 v217, 0x2a00, v213
	v_add_u32_e32 v218, 0xe00, v214
	v_add_u32_e32 v219, 0x1c00, v214
	v_add_u32_e32 v220, 0x2a00, v214
	v_add_u32_e32 v223, s54, v117
	v_add_u32_e32 v226, s54, v122
	v_sub_u32_e32 v228, v199, v126
	s_mov_b64 s[40:41], 0
	s_mov_b32 s55, 0xf149f2ca
	s_mov_b32 s56, 1.0
	s_movk_i32 s57, 0x46
	s_movk_i32 s58, 0x69
	v_mov_b32_e32 v232, 0x42200000
	s_mov_b32 s59, 0
	v_mov_b32_e32 v162, 0
	v_mov_b32_e32 v163, v114
	v_mov_b32_e32 v164, v114
	v_mov_b32_e32 v165, v114
	v_mov_b32_e32 v168, 0
	v_mov_b32_e32 v169, v114
	v_mov_b32_e32 v170, 0
	v_mov_b32_e32 v171, v114
	s_mov_b32 s75, 0
	s_branch .LBB1_43

.LBB1_55:
	s_or_saveexec_b64 s[24:25], s[24:25]
	v_mov_b32_e32 v116, 0
	v_lshlrev_b32_e32 v234, 1, v190
	v_lshlrev_b32_e32 v235, 1, v191
	v_mov_b32_e32 v117, 0
	v_mov_b32_e32 v166, 0
	v_mov_b32_e32 v167, 0
	v_mov_b32_e32 v150, 0
	v_mov_b32_e32 v151, 0
	v_mov_b32_e32 v152, 0
	v_mov_b32_e32 v153, 0
	v_mov_b32_e32 v174, 0
	v_mov_b32_e32 v175, 0
	v_mov_b32_e32 v172, 0
	v_mov_b32_e32 v173, 0
	s_xor_b64 exec, exec, s[24:25]
	s_cbranch_execz .LBB1_57
	s_lshl_b32 s42, s46, 1
	v_add_u32_e32 v115, s42, v199
	ds_read_b128 v[116:119], v115 offset:9216
	v_lshl_add_u32 v120, s46, 2, v198
	ds_read_b128 v[120:123], v120 offset:57600
	ds_read_b128 v[124:127], v115 offset:9344
	v_mad_u32_u24 v176, v233, s3, v227
	s_waitcnt lgkmcnt(6)
	v_mfma_f32_16x16x32_bf16 v[240:243], v[86:89], v[146:149], 0
	s_waitcnt lgkmcnt(0)
	v_mfma_f32_16x16x32_bf16 v[124:127], v[124:127], v[138:141], 0
	v_mfma_f32_16x16x32_bf16 v[116:119], v[116:119], v[146:149], v[120:123]
	s_nop 2
	ds_read_b128 v[120:123], v115 offset:9280
	ds_read_b128 v[128:131], v115 offset:9408
	v_mov_b32_e32 v115, s54
	v_mad_u32_u24 v162, v233, s53, v115
	v_add3_u32 v115, v162, v234, v235
	ds_read_b64 v[132:133], v115 offset:80
	s_waitcnt lgkmcnt(2)
	v_mfma_f32_16x16x32_bf16 v[118:121], v[120:123], v[142:145], v[116:119]
	v_mad_u32_u24 v115, v233, s52, v198
	ds_read_b128 v[150:153], v115 offset:60416
	v_mov_b32_e32 v115, s56
	s_waitcnt lgkmcnt(2)
	v_mfma_f32_16x16x32_bf16 v[122:125], v[128:131], v[134:137], v[124:127]
	s_waitcnt lgkmcnt(1)
	v_lshlrev_b32_e32 v116, 16, v132
	v_and_b32_e32 v117, 0xffff0000, v132
	v_lshlrev_b32_e32 v166, 16, v133
	v_and_b32_e32 v167, 0xffff0000, v133
	s_nop 2
	v_pk_add_f32 v[172:173], v[120:121], v[124:125]
	v_pk_add_f32 v[174:175], v[118:119], v[122:123]
	v_sub_f32_e32 v119, 1.0, v117
	v_sub_f32_e32 v118, 1.0, v116
	v_sub_f32_e32 v121, 1.0, v167
	v_sub_f32_e32 v120, 1.0, v166
	v_pk_mul_f32 v[120:121], v[172:173], v[120:121]
	v_pk_mul_f32 v[118:119], v[174:175], v[118:119]
	s_waitcnt lgkmcnt(0)
	v_pk_fma_f32 v[122:123], v[152:153], v[166:167], v[120:121]
	v_pk_fma_f32 v[124:125], v[150:151], v[116:117], v[118:119]
	v_mfma_f32_16x16x32_bf16 v[118:121], v[2:5], v[146:149], 0
	v_cndmask_b32_e64 v115, v123, v115, s[14:15]
	v_cndmask_b32_e64 v123, v122, v122, s[14:15]
	v_cndmask_b32_e64 v122, v125, v125, s[14:15]
	v_cndmask_b32_e64 v124, v124, v124, s[14:15]
	v_cvt_pk_bf16_f32 v122, v124, v122
	v_cvt_pk_bf16_f32 v123, v123, v115
	ds_write_b64 v200, v[122:123] offset:58112
	s_and_saveexec_b64 s[72:73], s[18:19]
	v_mov_b32_e32 v115, 0xe380
	ds_add_u32 v115, v115
	s_or_b64 exec, exec, s[72:73]
	v_mfma_f32_16x16x32_bf16 v[118:121], v[6:9], v[142:145], v[118:121]
	v_lshl_add_u32 v115, v192, 1, v162
	ds_read_b128 v[130:133], v115 offset:128
	ds_read_b128 v[236:239], v176 offset:2304
	v_add_u32_e32 v115, s42, v228
	ds_read_b128 v[162:165], v115 offset:39168
	ds_read_b128 v[244:247], v115 offset:39232
	v_mfma_f32_16x16x32_bf16 v[118:121], v[10:13], v[138:141], v[118:121]
	v_mfma_f32_16x16x32_bf16 v[118:121], v[14:17], v[134:137], v[118:121]
	s_waitcnt lgkmcnt(1)
	v_mfma_f32_16x16x32_bf16 v[162:165], v[162:165], v[236:239], 0
	ds_read_b128 v[236:239], v176 offset:2368
	v_mfma_f32_16x16x32_bf16 v[126:129], v[26:29], v[130:133], v[118:121]
	v_mfma_f32_16x16x32_bf16 v[118:121], v[30:33], v[146:149], 0
	v_mfma_f32_16x16x32_bf16 v[122:125], v[58:61], v[146:149], 0
	v_mfma_f32_16x16x32_bf16 v[118:121], v[34:37], v[142:145], v[118:121]
	v_mfma_f32_16x16x32_bf16 v[122:125], v[62:65], v[142:145], v[122:125]
	s_waitcnt lgkmcnt(0)
	v_mfma_f32_16x16x32_bf16 v[162:165], v[244:247], v[236:239], v[162:165]
	v_mov_b32_e32 v246, 0xe380
	ds_read_b32 v246, v246
	v_mfma_f32_16x16x32_bf16 v[236:239], v[90:93], v[142:145], v[240:243]
	v_mfma_f32_16x16x32_bf16 v[118:121], v[38:41], v[138:141], v[118:121]
	s_nop 5
	v_med3_f32 v115, v162, s55, 0
	v_exp_f32_e32 v162, v115
	v_med3_f32 v115, v163, s55, 0
	v_mfma_f32_16x16x32_bf16 v[122:125], v[66:69], v[138:141], v[122:125]
	v_exp_f32_e32 v163, v115
	v_med3_f32 v115, v164, s55, 0
	v_exp_f32_e32 v164, v115
	v_mfma_f32_16x16x32_bf16 v[236:239], v[94:97], v[138:141], v[236:239]
	v_med3_f32 v115, v165, s55, 0
	v_exp_f32_e32 v165, v115
	v_mfma_f32_16x16x32_bf16 v[118:121], v[42:45], v[134:137], v[118:121]
	v_mfma_f32_16x16x32_bf16 v[122:125], v[70:73], v[134:137], v[122:125]
	v_mfma_f32_16x16x32_bf16 v[236:239], v[98:101], v[134:137], v[236:239]
	v_mfma_f32_16x16x32_bf16 v[118:121], v[54:57], v[130:133], v[118:121]
	v_mfma_f32_16x16x32_bf16 v[122:125], v[82:85], v[130:133], v[122:125]
	v_mfma_f32_16x16x32_bf16 v[130:133], v[110:113], v[130:133], v[236:239]
.LBB1_57:
	s_or_b64 exec, exec, s[24:25]
	s_waitcnt lgkmcnt(0)
	s_and_saveexec_b64 s[24:25], s[6:7]
	s_xor_b64 s[24:25], exec, s[24:25]
	s_cbranch_execz .LBB1_68
	s_and_saveexec_b64 s[42:43], s[8:9]
	s_xor_b64 s[42:43], exec, s[42:43]
	s_cbranch_execz .LBB1_60
	v_mfma_f32_16x16x32_bf16 v[116:119], v[30:33], v[146:149], v[118:121]
	v_mad_u32_u24 v115, v233, s53, v226
	ds_read_b128 v[150:153], v115 offset:128
	v_lshl_add_u32 v115, s46, 1, v228
	v_mfma_f32_16x16x32_bf16 v[116:119], v[34:37], v[142:145], v[116:119]
	ds_read_b128 v[162:165], v115 offset:39168
	v_mfma_f32_16x16x32_bf16 v[116:119], v[38:41], v[138:141], v[116:119]
	v_mfma_f32_16x16x32_bf16 v[116:119], v[42:45], v[134:137], v[116:119]
	s_waitcnt lgkmcnt(1)
	v_mfma_f32_16x16x32_bf16 v[118:121], v[54:57], v[150:153], v[116:119]
	v_mfma_f32_16x16x32_bf16 v[126:129], v[2:5], v[146:149], v[126:129]
	s_nop 4
	v_mad_u32_u24 v116, v233, s3, v227
	ds_read_b128 v[172:175], v116 offset:2304
	v_mfma_f32_16x16x32_bf16 v[122:125], v[58:61], v[146:149], v[122:125]
	v_mfma_f32_16x16x32_bf16 v[130:133], v[86:89], v[146:149], v[130:133]
	ds_read_b128 v[146:149], v115 offset:39232
	v_mfma_f32_16x16x32_bf16 v[126:129], v[6:9], v[142:145], v[126:129]
	v_mfma_f32_16x16x32_bf16 v[122:125], v[62:65], v[142:145], v[122:125]
	s_waitcnt lgkmcnt(1)
	v_mfma_f32_16x16x32_bf16 v[162:165], v[162:165], v[172:175], 0
	ds_read_b128 v[172:175], v116 offset:2368
	v_mfma_f32_16x16x32_bf16 v[130:133], v[90:93], v[142:145], v[130:133]
	v_mfma_f32_16x16x32_bf16 v[126:129], v[10:13], v[138:141], v[126:129]
	v_mfma_f32_16x16x32_bf16 v[122:125], v[66:69], v[138:141], v[122:125]
	v_mfma_f32_16x16x32_bf16 v[130:133], v[94:97], v[138:141], v[130:133]
	s_waitcnt lgkmcnt(0)
	v_mfma_f32_16x16x32_bf16 v[146:149], v[146:149], v[172:175], v[162:165]
	v_mfma_f32_16x16x32_bf16 v[126:129], v[14:17], v[134:137], v[126:129]
	v_mfma_f32_16x16x32_bf16 v[122:125], v[70:73], v[134:137], v[122:125]
	s_nop 5
	v_med3_f32 v115, v146, s55, 0
	v_exp_f32_e32 v162, v115
	v_med3_f32 v115, v147, s55, 0
	v_mfma_f32_16x16x32_bf16 v[130:133], v[98:101], v[134:137], v[130:133]
	v_exp_f32_e32 v163, v115
	v_med3_f32 v115, v148, s55, 0
	v_exp_f32_e32 v164, v115
	v_mfma_f32_16x16x32_bf16 v[126:129], v[26:29], v[150:153], v[126:129]
	v_med3_f32 v115, v149, s55, 0
	v_exp_f32_e32 v165, v115
	v_mfma_f32_16x16x32_bf16 v[122:125], v[82:85], v[150:153], v[122:125]
	v_mfma_f32_16x16x32_bf16 v[130:133], v[110:113], v[150:153], v[130:133]

.LBB1_68:
	s_andn2_saveexec_b64 s[24:25], s[24:25]
	s_cbranch_execz .LBB1_80
	v_lshl_add_u32 v115, s46, 1, v228
	ds_read_b128 v[134:137], v115 offset:22272
	ds_read_b128 v[138:141], v115 offset:22336
	ds_read_b128 v[236:239], v203
	s_add_u32 s75, s75, 0x2aa80
	s_waitcnt lgkmcnt(3)
	v_readfirstlane_b32 s74, v246
	s_nop 1
	s_cmp_lt_u32 s74, s75
	s_cbranch_scc0 .Lpoll_done_0
.Lpoll_0:
	v_mov_b32_e32 v115, 0xe380
	ds_read_b32 v115, v115
	s_waitcnt lgkmcnt(0)
	v_readfirstlane_b32 s74, v115
	s_nop 1
	s_cmp_lt_u32 s74, s75
	s_cbranch_scc1 .Lpoll_0
.Lpoll_done_0:
	ds_read_b128 v[142:145], v202 offset:58112
	ds_read_b128 v[146:149], v202 offset:58176
	v_pk_mul_f32 v[176:177], v[166:167], v[152:153]
	v_pk_mul_f32 v[240:241], v[116:117], v[150:151]
	s_waitcnt lgkmcnt(1)
	v_mfma_f32_16x16x32_bf16 v[134:137], v[134:137], v[142:145], 0
	v_add_f32_e64 v242, -v116, 1.0
	v_add_f32_e64 v243, -v117, 1.0
	s_waitcnt lgkmcnt(0)
	v_pk_add_f32 v[144:145], v[236:237], 1.0 op_sel_hi:[1,0] neg_lo:[1,0] neg_hi:[1,0]
	v_mfma_f32_16x16x32_bf16 v[140:143], v[138:141], v[146:149], 0
	s_nop 7
	v_pk_add_f32 v[138:139], v[136:137], v[142:143]
	v_pk_add_f32 v[142:143], v[134:135], v[140:141]
	v_pk_mul_f32 v[136:137], v[238:239], v[138:139]
	v_pk_mul_f32 v[134:135], v[236:237], v[142:143]
	v_pk_add_f32 v[140:141], v[238:239], 1.0 op_sel_hi:[1,0] neg_lo:[1,0] neg_hi:[1,0]
	v_pk_fma_f32 v[144:145], v[174:175], v[144:145], v[134:135]
	v_pk_fma_f32 v[140:141], v[172:173], v[140:141], v[136:137]
	v_pk_add_f32 v[136:137], v[166:167], 1.0 op_sel_hi:[1,0] neg_lo:[1,0] neg_hi:[1,0]
	v_pk_fma_f32 v[134:135], v[242:243], v[144:145], v[240:241]
	v_pk_fma_f32 v[136:137], v[136:137], v[140:141], v[176:177]
	s_and_saveexec_b64 s[42:43], s[16:17]
	s_cbranch_execz .LBB1_71
	v_mov_b32_e32 v115, s56
	v_cndmask_b32_e64 v115, v137, v115, s[14:15]
	v_cndmask_b32_e64 v147, v136, v136, s[14:15]
	v_cndmask_b32_e64 v146, v135, v135, s[14:15]
	v_cndmask_b32_e64 v148, v134, v134, s[14:15]
	v_cvt_pk_bf16_f32 v146, v148, v146
	v_cvt_pk_bf16_f32 v147, v147, v115
	v_mad_u32_u24 v115, v233, s53, v204
	ds_write_b64 v115, v[146:147]

.LBB1_91:
	s_or_saveexec_b64 s[24:25], s[24:25]
	v_mov_b32_e32 v116, 0
	v_mov_b32_e32 v117, 0
	v_mov_b32_e32 v172, 0
	v_mov_b32_e32 v173, 0
	v_mov_b32_e32 v150, 0
	v_mov_b32_e32 v151, 0
	v_mov_b32_e32 v152, 0
	v_mov_b32_e32 v153, 0
	v_mov_b32_e32 v176, 0
	v_mov_b32_e32 v177, 0
	v_mov_b32_e32 v174, 0
	v_mov_b32_e32 v175, 0
	s_xor_b64 exec, exec, s[24:25]
	s_cbranch_execz .LBB1_93
	s_lshl_b32 s42, s46, 1
	v_add_u32_e32 v115, s42, v199
	ds_read_b128 v[116:119], v115 offset:9216
	v_lshl_add_u32 v120, s46, 2, v198
	ds_read_b128 v[120:123], v120 offset:57600
	ds_read_b128 v[124:127], v115 offset:9344
	v_mul_u32_u24_e32 v132, 0xe0, v233
	s_waitcnt lgkmcnt(6)
	v_mfma_f32_16x16x32_bf16 v[240:243], v[86:89], v[146:149], 0
	ds_read_b128 v[128:131], v115 offset:9408
	s_waitcnt lgkmcnt(2)
	v_mfma_f32_16x16x32_bf16 v[116:119], v[116:119], v[146:149], v[120:123]
	s_nop 2
	ds_read_b128 v[120:123], v115 offset:9280
	v_add_u32_e32 v115, s54, v132
	s_waitcnt lgkmcnt(2)
	v_mfma_f32_16x16x32_bf16 v[124:127], v[124:127], v[138:141], 0
	v_add_u32_e32 v162, 0xe00, v115
	v_add3_u32 v115, v162, v234, v235
	ds_read_b64 v[132:133], v115 offset:80
	s_waitcnt lgkmcnt(1)
	v_mfma_f32_16x16x32_bf16 v[118:121], v[120:123], v[142:145], v[116:119]
	v_mad_u32_u24 v115, v167, s52, v198
	ds_read_b128 v[150:153], v115 offset:60416
	s_waitcnt lgkmcnt(1)
	v_lshlrev_b32_e32 v116, 16, v132
	v_mfma_f32_16x16x32_bf16 v[122:125], v[128:131], v[134:137], v[124:127]
	v_and_b32_e32 v117, 0xffff0000, v132
	v_lshlrev_b32_e32 v172, 16, v133
	v_and_b32_e32 v173, 0xffff0000, v133
	v_mov_b32_e32 v115, s56
	s_nop 3
	v_pk_add_f32 v[174:175], v[120:121], v[124:125]
	v_pk_add_f32 v[176:177], v[118:119], v[122:123]
	v_sub_f32_e32 v119, 1.0, v117
	v_sub_f32_e32 v118, 1.0, v116
	v_sub_f32_e32 v121, 1.0, v173
	v_sub_f32_e32 v120, 1.0, v172
	v_pk_mul_f32 v[120:121], v[174:175], v[120:121]
	v_pk_mul_f32 v[118:119], v[176:177], v[118:119]
	s_waitcnt lgkmcnt(0)
	v_pk_fma_f32 v[122:123], v[152:153], v[172:173], v[120:121]
	v_pk_fma_f32 v[124:125], v[150:151], v[116:117], v[118:119]
	v_mfma_f32_16x16x32_bf16 v[118:121], v[2:5], v[146:149], 0
	v_cndmask_b32_e64 v115, v123, v115, s[14:15]
	v_cndmask_b32_e64 v123, v122, v122, s[14:15]
	v_cndmask_b32_e64 v122, v125, v125, s[14:15]
	v_cndmask_b32_e64 v124, v124, v124, s[14:15]
	v_cvt_pk_bf16_f32 v122, v124, v122
	v_cvt_pk_bf16_f32 v123, v123, v115
	ds_write_b64 v200, v[122:123] offset:58112
	s_and_saveexec_b64 s[72:73], s[18:19]
	v_mov_b32_e32 v115, 0xe380
	ds_add_u32 v115, v115
	s_or_b64 exec, exec, s[72:73]
	v_mfma_f32_16x16x32_bf16 v[118:121], v[6:9], v[142:145], v[118:121]
	v_lshl_add_u32 v115, v192, 1, v162
	ds_read_b128 v[130:133], v115 offset:128
	v_add_u32_e32 v115, s42, v228
	ds_read_b128 v[162:165], v115 offset:39168
	ds_read_b128 v[244:247], v115 offset:39232
	s_add_i32 s42, s33, 32
	s_and_b32 s42, s42, 0x60
	v_mfma_f32_16x16x32_bf16 v[118:121], v[10:13], v[138:141], v[118:121]
	v_or_b32_e32 v236, s42, v189
	v_mad_u32_u24 v248, v236, s3, v227
	ds_read_b128 v[236:239], v248
	v_mfma_f32_16x16x32_bf16 v[118:121], v[14:17], v[134:137], v[118:121]
	s_waitcnt lgkmcnt(0)
	v_mfma_f32_16x16x32_bf16 v[162:165], v[162:165], v[236:239], 0
	ds_read_b128 v[236:239], v248 offset:64
	v_mfma_f32_16x16x32_bf16 v[126:129], v[26:29], v[130:133], v[118:121]
	v_mfma_f32_16x16x32_bf16 v[118:121], v[30:33], v[146:149], 0
	v_mfma_f32_16x16x32_bf16 v[122:125], v[58:61], v[146:149], 0
	v_mfma_f32_16x16x32_bf16 v[118:121], v[34:37], v[142:145], v[118:121]
	v_mfma_f32_16x16x32_bf16 v[122:125], v[62:65], v[142:145], v[122:125]
	s_waitcnt lgkmcnt(0)
	v_mfma_f32_16x16x32_bf16 v[162:165], v[244:247], v[236:239], v[162:165]
	v_mov_b32_e32 v246, 0xe380
	ds_read_b32 v246, v246
	v_mfma_f32_16x16x32_bf16 v[236:239], v[90:93], v[142:145], v[240:243]
	v_mfma_f32_16x16x32_bf16 v[118:121], v[38:41], v[138:141], v[118:121]
	s_nop 5
	v_med3_f32 v115, v162, s55, 0
	v_exp_f32_e32 v162, v115
	v_med3_f32 v115, v163, s55, 0
	v_mfma_f32_16x16x32_bf16 v[122:125], v[66:69], v[138:141], v[122:125]
	v_exp_f32_e32 v163, v115
	v_med3_f32 v115, v164, s55, 0
	v_exp_f32_e32 v164, v115
	v_mfma_f32_16x16x32_bf16 v[236:239], v[94:97], v[138:141], v[236:239]
	v_med3_f32 v115, v165, s55, 0
	v_exp_f32_e32 v165, v115
	v_mfma_f32_16x16x32_bf16 v[118:121], v[42:45], v[134:137], v[118:121]
	v_mfma_f32_16x16x32_bf16 v[122:125], v[70:73], v[134:137], v[122:125]
	v_mfma_f32_16x16x32_bf16 v[236:239], v[98:101], v[134:137], v[236:239]
	v_mfma_f32_16x16x32_bf16 v[118:121], v[54:57], v[130:133], v[118:121]
	v_mfma_f32_16x16x32_bf16 v[122:125], v[82:85], v[130:133], v[122:125]
	v_mfma_f32_16x16x32_bf16 v[130:133], v[110:113], v[130:133], v[236:239]
.LBB1_93:
	s_or_b64 exec, exec, s[24:25]
	s_waitcnt lgkmcnt(0)
	s_and_saveexec_b64 s[24:25], s[6:7]
	s_xor_b64 s[24:25], exec, s[24:25]
	s_cbranch_execz .LBB1_104
	s_and_saveexec_b64 s[42:43], s[8:9]
	s_xor_b64 s[42:43], exec, s[42:43]
	s_cbranch_execz .LBB1_96
	v_mfma_f32_16x16x32_bf16 v[116:119], v[30:33], v[146:149], v[118:121]
	v_mad_u32_u24 v115, v167, s53, v226
	ds_read_b128 v[150:153], v115 offset:128
	v_lshl_add_u32 v115, s46, 1, v228
	v_mfma_f32_16x16x32_bf16 v[116:119], v[34:37], v[142:145], v[116:119]
	ds_read_b128 v[162:165], v115 offset:39168
	s_add_i32 s44, s33, 32
	s_and_b32 s44, s44, 0x60
	v_mfma_f32_16x16x32_bf16 v[116:119], v[38:41], v[138:141], v[116:119]
	v_mfma_f32_16x16x32_bf16 v[116:119], v[42:45], v[134:137], v[116:119]
	s_waitcnt lgkmcnt(1)
	v_mfma_f32_16x16x32_bf16 v[118:121], v[54:57], v[150:153], v[116:119]
	v_mfma_f32_16x16x32_bf16 v[126:129], v[2:5], v[146:149], v[126:129]
	s_nop 4
	v_or_b32_e32 v116, s44, v189
	v_mad_u32_u24 v116, v116, s3, v227
	ds_read_b128 v[172:175], v116
	v_mfma_f32_16x16x32_bf16 v[122:125], v[58:61], v[146:149], v[122:125]
	v_mfma_f32_16x16x32_bf16 v[130:133], v[86:89], v[146:149], v[130:133]
	ds_read_b128 v[146:149], v115 offset:39232
	v_mfma_f32_16x16x32_bf16 v[126:129], v[6:9], v[142:145], v[126:129]
	v_mfma_f32_16x16x32_bf16 v[122:125], v[62:65], v[142:145], v[122:125]
	s_waitcnt lgkmcnt(1)
	v_mfma_f32_16x16x32_bf16 v[162:165], v[162:165], v[172:175], 0
	ds_read_b128 v[172:175], v116 offset:64
	v_mfma_f32_16x16x32_bf16 v[130:133], v[90:93], v[142:145], v[130:133]
	v_mfma_f32_16x16x32_bf16 v[126:129], v[10:13], v[138:141], v[126:129]
	v_mfma_f32_16x16x32_bf16 v[122:125], v[66:69], v[138:141], v[122:125]
	v_mfma_f32_16x16x32_bf16 v[130:133], v[94:97], v[138:141], v[130:133]
	s_waitcnt lgkmcnt(0)
	v_mfma_f32_16x16x32_bf16 v[146:149], v[146:149], v[172:175], v[162:165]
	v_mfma_f32_16x16x32_bf16 v[126:129], v[14:17], v[134:137], v[126:129]
	v_mfma_f32_16x16x32_bf16 v[122:125], v[70:73], v[134:137], v[122:125]
	s_nop 5
	v_med3_f32 v115, v146, s55, 0
	v_exp_f32_e32 v162, v115
	v_med3_f32 v115, v147, s55, 0
	v_mfma_f32_16x16x32_bf16 v[130:133], v[98:101], v[134:137], v[130:133]
	v_exp_f32_e32 v163, v115
	v_med3_f32 v115, v148, s55, 0
	v_exp_f32_e32 v164, v115
	v_mfma_f32_16x16x32_bf16 v[126:129], v[26:29], v[150:153], v[126:129]
	v_med3_f32 v115, v149, s55, 0
	v_exp_f32_e32 v165, v115
	v_mfma_f32_16x16x32_bf16 v[122:125], v[82:85], v[150:153], v[122:125]
	v_mfma_f32_16x16x32_bf16 v[130:133], v[110:113], v[150:153], v[130:133]

.LBB1_104:
	s_andn2_saveexec_b64 s[24:25], s[24:25]
	s_cbranch_execz .LBB1_116
	v_lshl_add_u32 v115, s46, 1, v228
	ds_read_b128 v[134:137], v115 offset:22272
	ds_read_b128 v[138:141], v115 offset:22336
	ds_read_b128 v[236:239], v207 offset:3072
	s_add_u32 s75, s75, 0x2aa80
	s_waitcnt lgkmcnt(3)
	v_readfirstlane_b32 s74, v246
	s_nop 1
	s_cmp_lt_u32 s74, s75
	s_cbranch_scc0 .Lpoll_done_1

.Lpoll_done_1:
	ds_read_b128 v[142:145], v202 offset:58112
	ds_read_b128 v[146:149], v202 offset:58176
	v_pk_mul_f32 v[240:241], v[172:173], v[152:153]
	v_pk_mul_f32 v[242:243], v[116:117], v[150:151]
	s_waitcnt lgkmcnt(1)
	v_mfma_f32_16x16x32_bf16 v[134:137], v[134:137], v[142:145], 0
	v_add_f32_e64 v244, -v116, 1.0
	v_add_f32_e64 v245, -v117, 1.0
	s_waitcnt lgkmcnt(0)
	v_pk_add_f32 v[144:145], v[236:237], 1.0 op_sel_hi:[1,0] neg_lo:[1,0] neg_hi:[1,0]
	v_mfma_f32_16x16x32_bf16 v[140:143], v[138:141], v[146:149], 0
	s_nop 7
	v_pk_add_f32 v[138:139], v[136:137], v[142:143]
	v_pk_add_f32 v[142:143], v[134:135], v[140:141]
	v_pk_mul_f32 v[136:137], v[238:239], v[138:139]
	v_pk_mul_f32 v[134:135], v[236:237], v[142:143]
	v_pk_add_f32 v[140:141], v[238:239], 1.0 op_sel_hi:[1,0] neg_lo:[1,0] neg_hi:[1,0]
	v_pk_fma_f32 v[144:145], v[176:177], v[144:145], v[134:135]
	v_pk_fma_f32 v[140:141], v[174:175], v[140:141], v[136:137]
	v_pk_add_f32 v[136:137], v[172:173], 1.0 op_sel_hi:[1,0] neg_lo:[1,0] neg_hi:[1,0]
	v_pk_fma_f32 v[134:135], v[244:245], v[144:145], v[242:243]
	v_pk_fma_f32 v[136:137], v[136:137], v[140:141], v[240:241]
	s_and_saveexec_b64 s[42:43], s[16:17]
	s_cbranch_execz .LBB1_107
	v_mov_b32_e32 v115, s56
	v_cndmask_b32_e64 v115, v137, v115, s[14:15]
	v_cndmask_b32_e64 v147, v136, v136, s[14:15]
	v_cndmask_b32_e64 v146, v135, v135, s[14:15]
	v_cndmask_b32_e64 v148, v134, v134, s[14:15]
	v_cvt_pk_bf16_f32 v146, v148, v146
	v_cvt_pk_bf16_f32 v147, v147, v115
	v_mad_u32_u24 v115, v167, s53, v204
	ds_write_b64 v115, v[146:147]

.LBB1_127:
	s_or_saveexec_b64 s[24:25], s[24:25]
	v_mov_b32_e32 v116, 0
	v_mov_b32_e32 v117, 0
	v_mov_b32_e32 v172, 0
	v_mov_b32_e32 v173, 0
	v_mov_b32_e32 v150, 0
	v_mov_b32_e32 v151, 0
	v_mov_b32_e32 v152, 0
	v_mov_b32_e32 v153, 0
	v_mov_b32_e32 v176, 0
	v_mov_b32_e32 v177, 0
	v_mov_b32_e32 v174, 0
	v_mov_b32_e32 v175, 0
	s_xor_b64 exec, exec, s[24:25]
	s_cbranch_execz .LBB1_129
	s_lshl_b32 s42, s46, 1
	v_add_u32_e32 v115, s42, v199
	ds_read_b128 v[116:119], v115 offset:9216
	v_lshl_add_u32 v120, s46, 2, v198
	ds_read_b128 v[120:123], v120 offset:57600
	ds_read_b128 v[124:127], v115 offset:9344
	v_mul_u32_u24_e32 v132, 0xe0, v167
	s_waitcnt lgkmcnt(6)
	v_mfma_f32_16x16x32_bf16 v[242:245], v[86:89], v[146:149], 0
	ds_read_b128 v[128:131], v115 offset:9408
	s_waitcnt lgkmcnt(2)
	v_mfma_f32_16x16x32_bf16 v[116:119], v[116:119], v[146:149], v[120:123]
	s_nop 2
	ds_read_b128 v[120:123], v115 offset:9280
	v_add_u32_e32 v115, s54, v132
	s_waitcnt lgkmcnt(2)
	v_mfma_f32_16x16x32_bf16 v[124:127], v[124:127], v[138:141], 0
	v_add_u32_e32 v162, 0xe00, v115
	v_add3_u32 v115, v162, v234, v235
	ds_read_b64 v[132:133], v115 offset:80
	s_waitcnt lgkmcnt(1)
	v_mfma_f32_16x16x32_bf16 v[118:121], v[120:123], v[142:145], v[116:119]
	v_mad_u32_u24 v115, v236, s52, v198
	ds_read_b128 v[150:153], v115 offset:60416
	s_waitcnt lgkmcnt(1)
	v_lshlrev_b32_e32 v116, 16, v132
	v_mfma_f32_16x16x32_bf16 v[122:125], v[128:131], v[134:137], v[124:127]
	v_and_b32_e32 v117, 0xffff0000, v132
	v_lshlrev_b32_e32 v172, 16, v133
	v_and_b32_e32 v173, 0xffff0000, v133
	v_mov_b32_e32 v115, s56
	s_nop 3
	v_pk_add_f32 v[174:175], v[120:121], v[124:125]
	v_pk_add_f32 v[176:177], v[118:119], v[122:123]
	v_sub_f32_e32 v119, 1.0, v117
	v_sub_f32_e32 v118, 1.0, v116
	v_sub_f32_e32 v121, 1.0, v173
	v_sub_f32_e32 v120, 1.0, v172
	v_pk_mul_f32 v[120:121], v[174:175], v[120:121]
	v_pk_mul_f32 v[118:119], v[176:177], v[118:119]
	s_waitcnt lgkmcnt(0)
	v_pk_fma_f32 v[122:123], v[152:153], v[172:173], v[120:121]
	v_pk_fma_f32 v[124:125], v[150:151], v[116:117], v[118:119]
	v_mfma_f32_16x16x32_bf16 v[118:121], v[2:5], v[146:149], 0
	v_cndmask_b32_e64 v115, v123, v115, s[14:15]
	v_cndmask_b32_e64 v123, v122, v122, s[14:15]
	v_cndmask_b32_e64 v122, v125, v125, s[14:15]
	v_cndmask_b32_e64 v124, v124, v124, s[14:15]
	v_cvt_pk_bf16_f32 v122, v124, v122
	v_cvt_pk_bf16_f32 v123, v123, v115
	ds_write_b64 v200, v[122:123] offset:58112
	s_and_saveexec_b64 s[72:73], s[18:19]
	v_mov_b32_e32 v115, 0xe380
	ds_add_u32 v115, v115
	s_or_b64 exec, exec, s[72:73]
	v_mfma_f32_16x16x32_bf16 v[118:121], v[6:9], v[142:145], v[118:121]
	v_lshl_add_u32 v115, v192, 1, v162
	ds_read_b128 v[130:133], v115 offset:128
	v_add_u32_e32 v115, s42, v228
	ds_read_b128 v[162:165], v115 offset:39168
	ds_read_b128 v[246:249], v115 offset:39232
	s_add_i32 s42, s33, 32
	s_and_b32 s42, s42, 0x60
	v_mfma_f32_16x16x32_bf16 v[118:121], v[10:13], v[138:141], v[118:121]
	v_or_b32_e32 v167, s42, v189
	v_mad_u32_u24 v167, v167, s3, v227
	ds_read_b128 v[238:241], v167 offset:2304
	v_mfma_f32_16x16x32_bf16 v[118:121], v[14:17], v[134:137], v[118:121]
	s_waitcnt lgkmcnt(0)
	v_mfma_f32_16x16x32_bf16 v[162:165], v[162:165], v[238:241], 0
	ds_read_b128 v[238:241], v167 offset:2368
	v_mfma_f32_16x16x32_bf16 v[126:129], v[26:29], v[130:133], v[118:121]
	v_mfma_f32_16x16x32_bf16 v[118:121], v[30:33], v[146:149], 0
	v_mfma_f32_16x16x32_bf16 v[122:125], v[58:61], v[146:149], 0
	v_mfma_f32_16x16x32_bf16 v[118:121], v[34:37], v[142:145], v[118:121]
	v_mfma_f32_16x16x32_bf16 v[122:125], v[62:65], v[142:145], v[122:125]
	s_waitcnt lgkmcnt(0)
	v_mfma_f32_16x16x32_bf16 v[162:165], v[246:249], v[238:241], v[162:165]
	v_mov_b32_e32 v246, 0xe380
	ds_read_b32 v246, v246
	v_mfma_f32_16x16x32_bf16 v[238:241], v[90:93], v[142:145], v[242:245]
	v_mfma_f32_16x16x32_bf16 v[118:121], v[38:41], v[138:141], v[118:121]
	s_nop 5
	v_med3_f32 v115, v162, s55, 0
	v_exp_f32_e32 v162, v115
	v_med3_f32 v115, v163, s55, 0
	v_mfma_f32_16x16x32_bf16 v[122:125], v[66:69], v[138:141], v[122:125]
	v_exp_f32_e32 v163, v115
	v_med3_f32 v115, v164, s55, 0
	v_exp_f32_e32 v164, v115
	v_mfma_f32_16x16x32_bf16 v[238:241], v[94:97], v[138:141], v[238:241]
	v_med3_f32 v115, v165, s55, 0
	v_exp_f32_e32 v165, v115
	v_mfma_f32_16x16x32_bf16 v[118:121], v[42:45], v[134:137], v[118:121]
	v_mfma_f32_16x16x32_bf16 v[122:125], v[70:73], v[134:137], v[122:125]
	v_mfma_f32_16x16x32_bf16 v[238:241], v[98:101], v[134:137], v[238:241]
	v_mfma_f32_16x16x32_bf16 v[118:121], v[54:57], v[130:133], v[118:121]
	v_mfma_f32_16x16x32_bf16 v[122:125], v[82:85], v[130:133], v[122:125]
	v_mfma_f32_16x16x32_bf16 v[130:133], v[110:113], v[130:133], v[238:241]
.LBB1_129:
	s_or_b64 exec, exec, s[24:25]
	s_waitcnt lgkmcnt(0)
	s_and_saveexec_b64 s[24:25], s[6:7]
	s_xor_b64 s[24:25], exec, s[24:25]
	s_cbranch_execz .LBB1_140
	s_and_saveexec_b64 s[42:43], s[8:9]
	s_xor_b64 s[42:43], exec, s[42:43]
	s_cbranch_execz .LBB1_132
	v_mfma_f32_16x16x32_bf16 v[116:119], v[30:33], v[146:149], v[118:121]
	v_mad_u32_u24 v115, v236, s53, v226
	ds_read_b128 v[150:153], v115 offset:128
	v_lshl_add_u32 v115, s46, 1, v228
	v_mfma_f32_16x16x32_bf16 v[116:119], v[34:37], v[142:145], v[116:119]
	ds_read_b128 v[162:165], v115 offset:39168
	s_add_i32 s44, s33, 32
	s_and_b32 s44, s44, 0x60
	v_mfma_f32_16x16x32_bf16 v[116:119], v[38:41], v[138:141], v[116:119]
	v_mfma_f32_16x16x32_bf16 v[116:119], v[42:45], v[134:137], v[116:119]
	s_waitcnt lgkmcnt(1)
	v_mfma_f32_16x16x32_bf16 v[118:121], v[54:57], v[150:153], v[116:119]
	v_mfma_f32_16x16x32_bf16 v[126:129], v[2:5], v[146:149], v[126:129]
	s_nop 4
	v_or_b32_e32 v116, s44, v189
	v_mad_u32_u24 v116, v116, s3, v227
	ds_read_b128 v[172:175], v116 offset:2304
	v_mfma_f32_16x16x32_bf16 v[122:125], v[58:61], v[146:149], v[122:125]
	v_mfma_f32_16x16x32_bf16 v[130:133], v[86:89], v[146:149], v[130:133]
	ds_read_b128 v[146:149], v115 offset:39232
	v_mfma_f32_16x16x32_bf16 v[126:129], v[6:9], v[142:145], v[126:129]
	v_mfma_f32_16x16x32_bf16 v[122:125], v[62:65], v[142:145], v[122:125]
	s_waitcnt lgkmcnt(1)
	v_mfma_f32_16x16x32_bf16 v[162:165], v[162:165], v[172:175], 0
	ds_read_b128 v[172:175], v116 offset:2368
	v_mfma_f32_16x16x32_bf16 v[130:133], v[90:93], v[142:145], v[130:133]
	v_mfma_f32_16x16x32_bf16 v[126:129], v[10:13], v[138:141], v[126:129]
	v_mfma_f32_16x16x32_bf16 v[122:125], v[66:69], v[138:141], v[122:125]
	v_mfma_f32_16x16x32_bf16 v[130:133], v[94:97], v[138:141], v[130:133]
	s_waitcnt lgkmcnt(0)
	v_mfma_f32_16x16x32_bf16 v[146:149], v[146:149], v[172:175], v[162:165]
	v_mfma_f32_16x16x32_bf16 v[126:129], v[14:17], v[134:137], v[126:129]
	v_mfma_f32_16x16x32_bf16 v[122:125], v[70:73], v[134:137], v[122:125]
	s_nop 5
	v_med3_f32 v115, v146, s55, 0
	v_exp_f32_e32 v162, v115
	v_med3_f32 v115, v147, s55, 0
	v_mfma_f32_16x16x32_bf16 v[130:133], v[98:101], v[134:137], v[130:133]
	v_exp_f32_e32 v163, v115
	v_med3_f32 v115, v148, s55, 0
	v_exp_f32_e32 v164, v115
	v_mfma_f32_16x16x32_bf16 v[126:129], v[26:29], v[150:153], v[126:129]
	v_med3_f32 v115, v149, s55, 0
	v_exp_f32_e32 v165, v115
	v_mfma_f32_16x16x32_bf16 v[122:125], v[82:85], v[150:153], v[122:125]
	v_mfma_f32_16x16x32_bf16 v[130:133], v[110:113], v[150:153], v[130:133]

.LBB1_140:
	s_andn2_saveexec_b64 s[24:25], s[24:25]
	s_cbranch_execz .LBB1_152
	v_lshl_add_u32 v115, s46, 1, v228
	ds_read_b128 v[134:137], v115 offset:22272
	ds_read_b128 v[138:141], v115 offset:22336
	ds_read_b128 v[238:241], v207 offset:6144
	s_add_u32 s75, s75, 0x2aa80
	s_waitcnt lgkmcnt(3)
	v_readfirstlane_b32 s74, v246
	s_nop 1
	s_cmp_lt_u32 s74, s75
	s_cbranch_scc0 .Lpoll_done_2

.Lpoll_done_2:
	ds_read_b128 v[142:145], v202 offset:58112
	ds_read_b128 v[146:149], v202 offset:58176
	v_pk_mul_f32 v[242:243], v[172:173], v[152:153]
	v_pk_mul_f32 v[244:245], v[116:117], v[150:151]
	s_waitcnt lgkmcnt(1)
	v_mfma_f32_16x16x32_bf16 v[134:137], v[134:137], v[142:145], 0
	v_add_f32_e64 v246, -v116, 1.0
	v_add_f32_e64 v247, -v117, 1.0
	s_waitcnt lgkmcnt(0)
	v_pk_add_f32 v[144:145], v[238:239], 1.0 op_sel_hi:[1,0] neg_lo:[1,0] neg_hi:[1,0]
	v_mfma_f32_16x16x32_bf16 v[140:143], v[138:141], v[146:149], 0
	s_nop 7
	v_pk_add_f32 v[138:139], v[136:137], v[142:143]
	v_pk_add_f32 v[142:143], v[134:135], v[140:141]
	v_pk_mul_f32 v[136:137], v[240:241], v[138:139]
	v_pk_mul_f32 v[134:135], v[238:239], v[142:143]
	v_pk_add_f32 v[140:141], v[240:241], 1.0 op_sel_hi:[1,0] neg_lo:[1,0] neg_hi:[1,0]
	v_pk_fma_f32 v[144:145], v[176:177], v[144:145], v[134:135]
	v_pk_fma_f32 v[140:141], v[174:175], v[140:141], v[136:137]
	v_pk_add_f32 v[136:137], v[172:173], 1.0 op_sel_hi:[1,0] neg_lo:[1,0] neg_hi:[1,0]
	v_pk_fma_f32 v[134:135], v[246:247], v[144:145], v[244:245]
	v_pk_fma_f32 v[136:137], v[136:137], v[140:141], v[242:243]
	s_and_saveexec_b64 s[42:43], s[16:17]
	s_cbranch_execz .LBB1_143
	v_mov_b32_e32 v115, s56
	v_cndmask_b32_e64 v115, v137, v115, s[14:15]
	v_cndmask_b32_e64 v147, v136, v136, s[14:15]
	v_cndmask_b32_e64 v146, v135, v135, s[14:15]
	v_cndmask_b32_e64 v148, v134, v134, s[14:15]
	v_cvt_pk_bf16_f32 v146, v148, v146
	v_cvt_pk_bf16_f32 v147, v147, v115
	v_mad_u32_u24 v115, v236, s53, v204
	ds_write_b64 v115, v[146:147]

.LBB1_165:
	s_or_saveexec_b64 s[42:43], s[42:43]
	v_cndmask_b32_e64 v115, 0, 1, s[24:25]
	v_mov_b32_e32 v117, 0
	v_cmp_ne_u32_e64 s[24:25], 1, v115
	v_mov_b32_e32 v116, 0
	v_mov_b32_e32 v177, 0
	v_mov_b32_e32 v176, 0
	v_mov_b32_e32 v153, 0
	v_mov_b32_e32 v152, 0
	v_mov_b32_e32 v151, 0
	v_mov_b32_e32 v150, 0
	v_mov_b32_e32 v173, 0
	v_mov_b32_e32 v172, 0
	v_mov_b32_e32 v175, 0
	v_mov_b32_e32 v174, 0
	s_xor_b64 exec, exec, s[42:43]
	s_cbranch_execz .LBB1_169
	v_lshl_add_u32 v115, s48, 1, v199
	ds_read_b128 v[116:119], v115 offset:9216
	v_lshl_add_u32 v120, s48, 2, v198
	ds_read_b128 v[120:123], v120 offset:57600
	ds_read_b128 v[124:127], v115 offset:9344
	v_mul_u32_u24_e32 v132, 0xe0, v236
	s_and_b64 vcc, exec, s[24:25]
	s_waitcnt lgkmcnt(0)
	v_mfma_f32_16x16x32_bf16 v[124:127], v[124:127], v[142:145], 0
	ds_read_b128 v[128:131], v115 offset:9408
	v_mfma_f32_16x16x32_bf16 v[116:119], v[116:119], v[134:137], v[120:123]
	s_nop 2
	ds_read_b128 v[120:123], v115 offset:9280
	v_add_u32_e32 v115, s54, v132
	v_add_u32_e32 v132, 0xe00, v115
	v_add3_u32 v115, v132, v234, v235
	s_waitcnt lgkmcnt(0)
	v_mfma_f32_16x16x32_bf16 v[118:121], v[120:123], v[138:141], v[116:119]
	s_nop 2
	ds_read_b64 v[116:117], v115 offset:80
	v_mad_u32_u24 v115, v167, s52, v198
	ds_read_b128 v[150:153], v115 offset:60416
	v_mfma_f32_16x16x32_bf16 v[122:125], v[128:131], v[146:149], v[124:127]
	v_mov_b32_e32 v115, s56
	s_waitcnt lgkmcnt(1)
	v_lshlrev_b32_e32 v174, 16, v116
	v_and_b32_e32 v175, 0xffff0000, v116
	v_lshlrev_b32_e32 v172, 16, v117
	v_and_b32_e32 v173, 0xffff0000, v117
	s_nop 1
	v_pk_add_f32 v[116:117], v[120:121], v[124:125]
	v_pk_add_f32 v[176:177], v[118:119], v[122:123]
	v_sub_f32_e32 v119, 1.0, v173
	v_sub_f32_e32 v118, 1.0, v172
	v_sub_f32_e32 v121, 1.0, v175
	v_sub_f32_e32 v120, 1.0, v174
	v_pk_mul_f32 v[120:121], v[176:177], v[120:121]
	v_pk_mul_f32 v[118:119], v[116:117], v[118:119]
	s_waitcnt lgkmcnt(0)
	v_pk_fma_f32 v[124:125], v[150:151], v[174:175], v[120:121]
	v_pk_fma_f32 v[122:123], v[152:153], v[172:173], v[118:119]
	v_cndmask_b32_e64 v124, v124, v124, s[14:15]
	v_cndmask_b32_e64 v115, v123, v115, s[14:15]
	v_cndmask_b32_e64 v123, v122, v122, s[14:15]
	v_cndmask_b32_e64 v122, v125, v125, s[14:15]
	v_cvt_pk_bf16_f32 v122, v124, v122
	v_cvt_pk_bf16_f32 v123, v123, v115
	v_mfma_f32_16x16x32_bf16 v[118:121], v[2:5], v[134:137], 0
	ds_write_b64 v200, v[122:123] offset:58112
	s_and_saveexec_b64 s[72:73], s[18:19]
	v_mov_b32_e32 v115, 0xe380
	ds_add_u32 v115, v115
	s_or_b64 exec, exec, s[72:73]
	v_lshl_add_u32 v115, v192, 1, v132
	v_mfma_f32_16x16x32_bf16 v[122:125], v[30:33], v[134:137], 0
	ds_read_b128 v[130:133], v115 offset:128
	v_mfma_f32_16x16x32_bf16 v[126:129], v[58:61], v[134:137], 0
	v_mfma_f32_16x16x32_bf16 v[234:237], v[86:89], v[134:137], 0
	v_mfma_f32_16x16x32_bf16 v[118:121], v[6:9], v[138:141], v[118:121]
	v_mfma_f32_16x16x32_bf16 v[122:125], v[34:37], v[138:141], v[122:125]
	v_mfma_f32_16x16x32_bf16 v[126:129], v[62:65], v[138:141], v[126:129]
	v_mfma_f32_16x16x32_bf16 v[234:237], v[90:93], v[138:141], v[234:237]
	v_mfma_f32_16x16x32_bf16 v[118:121], v[10:13], v[142:145], v[118:121]
	v_mfma_f32_16x16x32_bf16 v[122:125], v[38:41], v[142:145], v[122:125]
	v_mfma_f32_16x16x32_bf16 v[126:129], v[66:69], v[142:145], v[126:129]
	v_mfma_f32_16x16x32_bf16 v[234:237], v[94:97], v[142:145], v[234:237]
	v_mfma_f32_16x16x32_bf16 v[118:121], v[14:17], v[146:149], v[118:121]
	v_mfma_f32_16x16x32_bf16 v[122:125], v[42:45], v[146:149], v[122:125]
	v_mfma_f32_16x16x32_bf16 v[126:129], v[70:73], v[146:149], v[126:129]
	v_mfma_f32_16x16x32_bf16 v[234:237], v[98:101], v[146:149], v[234:237]
	s_waitcnt lgkmcnt(0)
	v_mfma_f32_16x16x32_bf16 v[118:121], v[26:29], v[130:133], v[118:121]
	v_mov_b32_e32 v246, 0xe380
	ds_read_b32 v246, v246
	v_mfma_f32_16x16x32_bf16 v[122:125], v[54:57], v[130:133], v[122:125]
	v_mfma_f32_16x16x32_bf16 v[126:129], v[82:85], v[130:133], v[126:129]
	v_mfma_f32_16x16x32_bf16 v[130:133], v[110:113], v[130:133], v[234:237]
	s_cbranch_vccnz .LBB1_168
	v_lshl_add_u32 v115, s48, 1, v228
	ds_read_b128 v[162:165], v115 offset:39168
	s_add_i32 s44, s33, 64
	v_and_or_b32 v233, s44, 64, v189
	v_mad_u32_u24 v233, v233, s3, v227
	ds_read_b128 v[234:237], v115 offset:39232
	ds_read_b128 v[238:241], v233
	ds_read_b128 v[242:245], v233 offset:64
	s_waitcnt lgkmcnt(1)
	v_mfma_f32_16x16x32_bf16 v[162:165], v[162:165], v[238:241], 0
	s_waitcnt lgkmcnt(0)
	v_mfma_f32_16x16x32_bf16 v[162:165], v[234:237], v[242:245], v[162:165]
	s_nop 7
	v_med3_f32 v115, v162, s55, 0
	v_med3_f32 v163, v163, s55, 0
	v_med3_f32 v164, v164, s55, 0
	v_med3_f32 v165, v165, s55, 0
	v_exp_f32_e32 v162, v115
	v_exp_f32_e32 v163, v163
	v_exp_f32_e32 v164, v164
	v_exp_f32_e32 v165, v165
.LBB1_168:
.LBB1_169:
	s_or_b64 exec, exec, s[42:43]
	s_waitcnt lgkmcnt(0)
	s_and_saveexec_b64 s[42:43], s[6:7]
	s_xor_b64 s[42:43], exec, s[42:43]
	s_cbranch_execz .LBB1_180
	s_and_saveexec_b64 s[44:45], s[8:9]
	s_xor_b64 s[44:45], exec, s[44:45]
	s_cbranch_execz .LBB1_174
	v_mfma_f32_16x16x32_bf16 v[116:119], v[2:5], v[134:137], v[118:121]
	v_mad_u32_u24 v115, v167, s53, v226
	ds_read_b128 v[150:153], v115 offset:128
	s_and_b64 vcc, exec, s[24:25]
	v_mfma_f32_16x16x32_bf16 v[122:125], v[30:33], v[134:137], v[122:125]
	v_mfma_f32_16x16x32_bf16 v[126:129], v[58:61], v[134:137], v[126:129]
	v_mfma_f32_16x16x32_bf16 v[130:133], v[86:89], v[134:137], v[130:133]
	v_mfma_f32_16x16x32_bf16 v[116:119], v[6:9], v[138:141], v[116:119]
	v_mfma_f32_16x16x32_bf16 v[122:125], v[34:37], v[138:141], v[122:125]
	v_mfma_f32_16x16x32_bf16 v[126:129], v[62:65], v[138:141], v[126:129]
	v_mfma_f32_16x16x32_bf16 v[130:133], v[90:93], v[138:141], v[130:133]
	v_mfma_f32_16x16x32_bf16 v[116:119], v[10:13], v[142:145], v[116:119]
	v_mfma_f32_16x16x32_bf16 v[122:125], v[38:41], v[142:145], v[122:125]
	v_mfma_f32_16x16x32_bf16 v[126:129], v[66:69], v[142:145], v[126:129]
	v_mfma_f32_16x16x32_bf16 v[130:133], v[94:97], v[142:145], v[130:133]
	v_mfma_f32_16x16x32_bf16 v[116:119], v[14:17], v[146:149], v[116:119]
	v_mfma_f32_16x16x32_bf16 v[122:125], v[42:45], v[146:149], v[122:125]
	v_mfma_f32_16x16x32_bf16 v[126:129], v[70:73], v[146:149], v[126:129]
	v_mfma_f32_16x16x32_bf16 v[130:133], v[98:101], v[146:149], v[130:133]
	s_waitcnt lgkmcnt(0)
	v_mfma_f32_16x16x32_bf16 v[118:121], v[26:29], v[150:153], v[116:119]
	v_mfma_f32_16x16x32_bf16 v[122:125], v[54:57], v[150:153], v[122:125]
	v_mfma_f32_16x16x32_bf16 v[126:129], v[82:85], v[150:153], v[126:129]
	v_mfma_f32_16x16x32_bf16 v[130:133], v[110:113], v[150:153], v[130:133]
	s_cbranch_vccnz .LBB1_173
	v_lshl_add_u32 v115, s48, 1, v228
	ds_read_b128 v[134:137], v115 offset:39168
	s_add_i32 s46, s33, 64
	v_and_or_b32 v116, s46, 64, v189
	v_mad_u32_u24 v116, v116, s3, v227
	ds_read_b128 v[138:141], v115 offset:39232
	ds_read_b128 v[142:145], v116
	ds_read_b128 v[146:149], v116 offset:64
	s_waitcnt lgkmcnt(1)
	v_mfma_f32_16x16x32_bf16 v[134:137], v[134:137], v[142:145], 0
	s_waitcnt lgkmcnt(0)
	v_mfma_f32_16x16x32_bf16 v[134:137], v[138:141], v[146:149], v[134:137]
	s_nop 7
	v_med3_f32 v115, v134, s55, 0
	v_med3_f32 v116, v135, s55, 0
	v_med3_f32 v117, v136, s55, 0
	v_med3_f32 v134, v137, s55, 0
	v_exp_f32_e32 v162, v115
	v_exp_f32_e32 v163, v116
	v_exp_f32_e32 v164, v117
	v_exp_f32_e32 v165, v134

.LBB1_180:
	s_andn2_saveexec_b64 s[42:43], s[42:43]
	s_cbranch_execz .LBB1_192
	v_lshl_add_u32 v115, s48, 1, v228
	ds_read_b128 v[134:137], v115 offset:22272
	ds_read_b128 v[138:141], v115 offset:22336
	ds_read_b128 v[234:237], v207 offset:9216
	s_add_u32 s75, s75, 0x2aa80
	s_waitcnt lgkmcnt(3)
	v_readfirstlane_b32 s74, v246
	s_nop 1
	s_cmp_lt_u32 s74, s75
	s_cbranch_scc0 .Lpoll_done_3

.Lpoll_done_3:
	ds_read_b128 v[142:145], v202 offset:58112
	ds_read_b128 v[146:149], v202 offset:58176
	v_pk_mul_f32 v[238:239], v[172:173], v[152:153]
	v_pk_mul_f32 v[240:241], v[174:175], v[150:151]
	s_waitcnt lgkmcnt(1)
	v_mfma_f32_16x16x32_bf16 v[134:137], v[134:137], v[142:145], 0
	v_add_f32_e64 v242, -v174, 1.0
	v_add_f32_e64 v243, -v175, 1.0
	s_waitcnt lgkmcnt(0)
	v_pk_add_f32 v[144:145], v[234:235], 1.0 op_sel_hi:[1,0] neg_lo:[1,0] neg_hi:[1,0]
	v_mfma_f32_16x16x32_bf16 v[140:143], v[138:141], v[146:149], 0
	s_nop 7
	v_pk_add_f32 v[138:139], v[136:137], v[142:143]
	v_pk_add_f32 v[142:143], v[134:135], v[140:141]
	v_pk_mul_f32 v[136:137], v[236:237], v[138:139]
	v_pk_mul_f32 v[134:135], v[234:235], v[142:143]
	v_pk_add_f32 v[140:141], v[236:237], 1.0 op_sel_hi:[1,0] neg_lo:[1,0] neg_hi:[1,0]
	v_pk_fma_f32 v[144:145], v[176:177], v[144:145], v[134:135]
	v_pk_fma_f32 v[140:141], v[116:117], v[140:141], v[136:137]
	v_pk_add_f32 v[136:137], v[172:173], 1.0 op_sel_hi:[1,0] neg_lo:[1,0] neg_hi:[1,0]
	v_pk_fma_f32 v[134:135], v[242:243], v[144:145], v[240:241]
	v_pk_fma_f32 v[136:137], v[136:137], v[140:141], v[238:239]
	s_and_saveexec_b64 s[44:45], s[16:17]
	s_cbranch_execz .LBB1_183
	v_mov_b32_e32 v115, s56
	v_cndmask_b32_e64 v115, v137, v115, s[14:15]
	v_cndmask_b32_e64 v147, v136, v136, s[14:15]
	v_cndmask_b32_e64 v146, v135, v135, s[14:15]
	v_cndmask_b32_e64 v148, v134, v134, s[14:15]
	v_cvt_pk_bf16_f32 v146, v148, v146
	v_cvt_pk_bf16_f32 v147, v147, v115
	v_mad_u32_u24 v115, v167, s53, v204
	ds_write_b64 v115, v[146:147]

	.amdhsa_kernel _Z10rnn_kernelPKfS0_S0_S0_S0_S0_PKtS2_PfPtS3_
		.amdhsa_group_segment_fixed_size 0
		.amdhsa_private_segment_fixed_size 0
		.amdhsa_kernarg_size 88
		.amdhsa_user_sgpr_count 2
		.amdhsa_user_sgpr_dispatch_ptr 0
		.amdhsa_user_sgpr_queue_ptr 0
		.amdhsa_user_sgpr_kernarg_segment_ptr 1
		.amdhsa_user_sgpr_dispatch_id 0
		.amdhsa_user_sgpr_kernarg_preload_length 0
		.amdhsa_user_sgpr_kernarg_preload_offset 0
		.amdhsa_user_sgpr_private_segment_size 0
		.amdhsa_uses_dynamic_stack 0
		.amdhsa_enable_private_segment 0
		.amdhsa_system_sgpr_workgroup_id_x 1
		.amdhsa_system_sgpr_workgroup_id_y 0
		.amdhsa_system_sgpr_workgroup_id_z 0
		.amdhsa_system_sgpr_workgroup_info 0
		.amdhsa_system_vgpr_workitem_id 0
		.amdhsa_next_free_vgpr 250
		.amdhsa_next_free_sgpr 76
		.amdhsa_accum_offset 252
		.amdhsa_reserve_vcc 1
		.amdhsa_float_round_mode_32 0
		.amdhsa_float_round_mode_16_64 0
		.amdhsa_float_denorm_mode_32 3
		.amdhsa_float_denorm_mode_16_64 3
		.amdhsa_dx10_clamp 1
		.amdhsa_ieee_mode 1
		.amdhsa_fp16_overflow 0
		.amdhsa_tg_split 0
		.amdhsa_exception_fp_ieee_invalid_op 0
		.amdhsa_exception_fp_denorm_src 0
		.amdhsa_exception_fp_ieee_div_zero 0
		.amdhsa_exception_fp_ieee_overflow 0
		.amdhsa_exception_fp_ieee_underflow 0
		.amdhsa_exception_fp_ieee_inexact 0
		.amdhsa_exception_int_div_zero 0
	.end_amdhsa_kernel

amdhsa.kernels:
  - .agpr_count:     0
    .args:
      - .actual_access:  read_only
        .address_space:  global
        .offset:         0
        .size:           8
        .value_kind:     global_buffer
      - .actual_access:  read_only
        .address_space:  global
        .offset:         8
        .size:           8
        .value_kind:     global_buffer
      - .actual_access:  read_only
        .address_space:  global
        .offset:         16
        .size:           8
        .value_kind:     global_buffer
      - .actual_access:  read_only
        .address_space:  global
        .offset:         24
        .size:           8
        .value_kind:     global_buffer
      - .actual_access:  read_only
        .address_space:  global
        .offset:         32
        .size:           8
        .value_kind:     global_buffer
      - .actual_access:  read_only
        .address_space:  global
        .offset:         40
        .size:           8
        .value_kind:     global_buffer
      - .actual_access:  read_only
        .address_space:  global
        .offset:         48
        .size:           8
        .value_kind:     global_buffer
      - .actual_access:  read_only
        .address_space:  global
        .offset:         56
        .size:           8
        .value_kind:     global_buffer
      - .actual_access:  read_only
        .address_space:  global
        .offset:         64
        .size:           8
        .value_kind:     global_buffer
      - .actual_access:  read_only
        .address_space:  global
        .offset:         72
        .size:           8
        .value_kind:     global_buffer
      - .actual_access:  read_only
        .address_space:  global
        .offset:         80
        .size:           8
        .value_kind:     global_buffer
      - .actual_access:  read_only
        .address_space:  global
        .offset:         88
        .size:           8
        .value_kind:     global_buffer
      - .actual_access:  read_only
        .address_space:  global
        .offset:         96
        .size:           8
        .value_kind:     global_buffer
      - .actual_access:  read_only
        .address_space:  global
        .offset:         104
        .size:           8
        .value_kind:     global_buffer
      - .actual_access:  read_only
        .address_space:  global
        .offset:         112
        .size:           8
        .value_kind:     global_buffer
      - .actual_access:  read_only
        .address_space:  global
        .offset:         120
        .size:           8
        .value_kind:     global_buffer
      - .actual_access:  write_only
        .address_space:  global
        .offset:         128
        .size:           8
        .value_kind:     global_buffer
      - .actual_access:  write_only
        .address_space:  global
        .offset:         136
        .size:           8
        .value_kind:     global_buffer
      - .actual_access:  write_only
        .address_space:  global
        .offset:         144
        .size:           8
        .value_kind:     global_buffer
    .group_segment_fixed_size: 0
    .kernarg_segment_align: 8
    .kernarg_segment_size: 152
    .language:       OpenCL C
    .language_version:
      - 2
      - 0
    .max_flat_workgroup_size: 256
    .name:           _Z11prep_kernelPKfS0_S0_S0_S0_S0_S0_S0_S0_S0_S0_S0_S0_S0_S0_S0_PtS1_S1_
    .private_segment_fixed_size: 0
    .sgpr_count:     30
    .sgpr_spill_count: 0
    .symbol:         _Z11prep_kernelPKfS0_S0_S0_S0_S0_S0_S0_S0_S0_S0_S0_S0_S0_S0_S0_PtS1_S1_.kd
    .uniform_work_group_size: 1
    .uses_dynamic_stack: false
    .vgpr_count:     8
    .vgpr_spill_count: 0
    .wavefront_size: 64
  - .agpr_count:     0
    .args:
      - .actual_access:  read_only
        .address_space:  global
        .offset:         0
        .size:           8
        .value_kind:     global_buffer
      - .actual_access:  read_only
        .address_space:  global
        .offset:         8
        .size:           8
        .value_kind:     global_buffer
      - .actual_access:  read_only
        .address_space:  global
        .offset:         16
        .size:           8
        .value_kind:     global_buffer
      - .actual_access:  read_only
        .address_space:  global
        .offset:         24
        .size:           8
        .value_kind:     global_buffer
      - .actual_access:  read_only
        .address_space:  global
        .offset:         32
        .size:           8
        .value_kind:     global_buffer
      - .actual_access:  read_only
        .address_space:  global
        .offset:         40
        .size:           8
        .value_kind:     global_buffer
      - .actual_access:  read_only
        .address_space:  global
        .offset:         48
        .size:           8
        .value_kind:     global_buffer
      - .actual_access:  read_only
        .address_space:  global
        .offset:         56
        .size:           8
        .value_kind:     global_buffer
      - .actual_access:  write_only
        .address_space:  global
        .offset:         64
        .size:           8
        .value_kind:     global_buffer
      - .actual_access:  write_only
        .address_space:  global
        .offset:         72
        .size:           8
        .value_kind:     global_buffer
      - .actual_access:  write_only
        .address_space:  global
        .offset:         80
        .size:           8
        .value_kind:     global_buffer
    .group_segment_fixed_size: 0
    .kernarg_segment_align: 8
    .kernarg_segment_size: 88
    .language:       OpenCL C
    .language_version:
      - 2
      - 0
    .max_flat_workgroup_size: 512
    .name:           _Z10rnn_kernelPKfS0_S0_S0_S0_S0_PKtS2_PfPtS3_
    .private_segment_fixed_size: 0
    .sgpr_count:     82
    .sgpr_spill_count: 0
    .symbol:         _Z10rnn_kernelPKfS0_S0_S0_S0_S0_PKtS2_PfPtS3_.kd
    .uniform_work_group_size: 1
    .uses_dynamic_stack: false
    .vgpr_count:     250
    .vgpr_spill_count: 0
    .wavefront_size: 64
  - .agpr_count:     0
    .args:
      - .actual_access:  read_only
        .address_space:  global
        .offset:         0
        .size:           8
        .value_kind:     global_buffer
      - .actual_access:  read_only
        .address_space:  global
        .offset:         8
        .size:           8
        .value_kind:     global_buffer
      - .actual_access:  read_only
        .address_space:  global
        .offset:         16
        .size:           8
        .value_kind:     global_buffer
      - .actual_access:  read_only
        .address_space:  global
        .offset:         24
        .size:           8
        .value_kind:     global_buffer
      - .actual_access:  read_only
        .address_space:  global
        .offset:         32
        .size:           8
        .value_kind:     global_buffer
      - .actual_access:  write_only
        .address_space:  global
        .offset:         40
        .size:           8
        .value_kind:     global_buffer
      - .actual_access:  write_only
        .address_space:  global
        .offset:         48
        .size:           8
        .value_kind:     global_buffer
    .group_segment_fixed_size: 0
    .kernarg_segment_align: 8
    .kernarg_segment_size: 56
    .language:       OpenCL C
    .language_version:
      - 2
      - 0
    .max_flat_workgroup_size: 1024
    .name:           _Z11attn_kernelPKtS0_PKfS2_S2_PfS3_
    .private_segment_fixed_size: 0
    .sgpr_count:     30
    .sgpr_spill_count: 0
    .symbol:         _Z11attn_kernelPKtS0_PKfS2_S2_PfS3_.kd
    .uniform_work_group_size: 1
    .uses_dynamic_stack: false
    .vgpr_count:     124
    .vgpr_spill_count: 0
    .wavefront_size: 64
  - .agpr_count:     0
    .args:
      - .actual_access:  read_only
        .address_space:  global
        .offset:         0
        .size:           8
        .value_kind:     global_buffer
      - .actual_access:  read_only
        .address_space:  global
        .offset:         8
        .size:           8
        .value_kind:     global_buffer
      - .actual_access:  read_only
        .address_space:  global
        .offset:         16
        .size:           8
        .value_kind:     global_buffer
      - .actual_access:  write_only
        .address_space:  global
        .offset:         24
        .size:           8
        .value_kind:     global_buffer
    .group_segment_fixed_size: 192
    .kernarg_segment_align: 8
    .kernarg_segment_size: 32
    .language:       OpenCL C
    .language_version:
      - 2
      - 0
    .max_flat_workgroup_size: 1024
    .name:           _Z11loss_kernelPKfS0_S0_Pf
    .private_segment_fixed_size: 0
    .sgpr_count:     14
    .sgpr_spill_count: 0
    .symbol:         _Z11loss_kernelPKfS0_S0_Pf.kd
    .uniform_work_group_size: 1
    .uses_dynamic_stack: false
    .vgpr_count:     46
    .vgpr_spill_count: 0
    .wavefront_size: 64
